# nt (non-temporal) hint on the gemm_in epilogue stores of U
# speedup vs baseline: 1.0572x; 1.0012x over previous
.LBB0_158:
	s_add_u32 s22, s16, s4
	s_addc_u32 s23, s17, s5
	s_add_u32 s24, s22, 0x4578100
	s_addc_u32 s25, s23, 0
	s_add_u32 s45, s15, s4
	s_addc_u32 s46, s43, s5
	s_cmpk_eq_i32 s4, 0x700
	s_cselect_b64 vcc, -1, 0
	s_and_b64 s[22:23], vcc, exec
	s_cselect_b32 s25, s7, s25
	s_cselect_b32 s24, s6, s24
	s_cselect_b32 s23, s0, s46
	s_cselect_b32 s22, s1, s45
	s_add_i32 s45, 0, 0x10000
	v_add_u32_e32 v163, s45, v139
	ds_read_b128 v[158:161], v163
	ds_read_b128 v[170:173], v163 offset:1024
	ds_read_b128 v[174:177], v163 offset:2048
	ds_read_b128 v[178:181], v163 offset:3072
	v_cndmask_b32_e32 v34, v136, v154, vcc
	v_cndmask_b32_e32 v141, v140, v156, vcc
	v_cndmask_b32_e32 v162, v138, v155, vcc
	v_cndmask_b32_e32 v143, v142, v157, vcc
	v_lshl_add_u64 v[198:199], v[146:147], 0, s[4:5]
	s_add_i32 m0, s31, 0xc000
	ds_read_b128 v[182:185], v153
	ds_read_b128 v[186:189], v153 offset:1024
	ds_read_b128 v[190:193], v153 offset:2048
	ds_read_b128 v[194:197], v153 offset:3072
	ds_read_b128 v[204:207], v153 offset:4096
	ds_read_b128 v[208:211], v153 offset:5120
	ds_read_b128 v[212:215], v153 offset:6144
	ds_read_b128 v[216:219], v153 offset:7168
	global_load_lds_dwordx4 v[198:199], off
	v_lshl_add_u64 v[198:199], v[144:145], 0, s[4:5]
	s_add_i32 m0, s31, 0xe000
	s_nop 0
	global_load_lds_dwordx4 v[198:199], off
	s_waitcnt lgkmcnt(8)
	s_barrier
	s_waitcnt lgkmcnt(0)
	s_setprio 1
	s_waitcnt lgkmcnt(0)
	v_mfma_f32_16x16x32_bf16 v[128:131], v[158:161], v[182:185], v[128:131]
	v_mfma_f32_16x16x32_bf16 v[124:127], v[174:177], v[182:185], v[124:127]
	v_mfma_f32_16x16x32_bf16 v[120:123], v[158:161], v[190:193], v[120:123]
	v_mfma_f32_16x16x32_bf16 v[116:119], v[174:177], v[190:193], v[116:119]
	v_mfma_f32_16x16x32_bf16 v[104:107], v[158:161], v[204:207], v[104:107]
	v_mfma_f32_16x16x32_bf16 v[100:103], v[174:177], v[204:207], v[100:103]
	v_mfma_f32_16x16x32_bf16 v[88:91], v[158:161], v[212:215], v[88:91]
	v_mfma_f32_16x16x32_bf16 v[84:87], v[174:177], v[212:215], v[84:87]
	v_mfma_f32_16x16x32_bf16 v[128:131], v[170:173], v[186:189], v[128:131]
	v_mfma_f32_16x16x32_bf16 v[124:127], v[178:181], v[186:189], v[124:127]
	v_mfma_f32_16x16x32_bf16 v[120:123], v[170:173], v[194:197], v[120:123]
	v_mfma_f32_16x16x32_bf16 v[116:119], v[178:181], v[194:197], v[116:119]
	v_mfma_f32_16x16x32_bf16 v[104:107], v[170:173], v[208:211], v[104:107]
	v_mfma_f32_16x16x32_bf16 v[100:103], v[178:181], v[208:211], v[100:103]
	v_mfma_f32_16x16x32_bf16 v[88:91], v[170:173], v[216:219], v[88:91]
	v_mfma_f32_16x16x32_bf16 v[84:87], v[178:181], v[216:219], v[84:87]
	s_setprio 0
	s_barrier
	s_add_i32 s48, 0, 0x14000
	s_add_i32 s45, s45, s30
	v_add_u32_e32 v163, s48, v139
	v_lshl_add_u64 v[198:199], s[22:23], 0, v[132:133]
	s_mov_b32 m0, s45
	ds_read_b128 v[220:223], v163
	ds_read_b128 v[224:227], v163 offset:1024
	ds_read_b128 v[228:231], v163 offset:2048
	ds_read_b128 v[232:235], v163 offset:3072
	global_load_lds_dwordx4 v[198:199], off
	v_lshl_add_u64 v[236:237], s[22:23], 0, v[134:135]
	s_add_i32 m0, s45, 0x2000
	s_nop 0
	global_load_lds_dwordx4 v[236:237], off
	s_barrier
	s_waitcnt lgkmcnt(0)
	s_setprio 1
	s_waitcnt lgkmcnt(0)
	v_mfma_f32_16x16x32_bf16 v[112:115], v[220:223], v[182:185], v[112:115]
	v_mfma_f32_16x16x32_bf16 v[108:111], v[228:231], v[182:185], v[108:111]
	v_mfma_f32_16x16x32_bf16 v[96:99], v[220:223], v[190:193], v[96:99]
	v_mfma_f32_16x16x32_bf16 v[92:95], v[228:231], v[190:193], v[92:95]
	v_mfma_f32_16x16x32_bf16 v[80:83], v[220:223], v[204:207], v[80:83]
	v_mfma_f32_16x16x32_bf16 v[76:79], v[228:231], v[204:207], v[76:79]
	v_mfma_f32_16x16x32_bf16 v[72:75], v[220:223], v[212:215], v[72:75]
	v_mfma_f32_16x16x32_bf16 v[68:71], v[228:231], v[212:215], v[68:71]
	v_mfma_f32_16x16x32_bf16 v[112:115], v[224:227], v[186:189], v[112:115]
	v_mfma_f32_16x16x32_bf16 v[108:111], v[232:235], v[186:189], v[108:111]
	v_mfma_f32_16x16x32_bf16 v[96:99], v[224:227], v[194:197], v[96:99]
	v_mfma_f32_16x16x32_bf16 v[92:95], v[232:235], v[194:197], v[92:95]
	v_mfma_f32_16x16x32_bf16 v[80:83], v[224:227], v[208:211], v[80:83]
	v_mfma_f32_16x16x32_bf16 v[76:79], v[232:235], v[208:211], v[76:79]
	v_mfma_f32_16x16x32_bf16 v[72:75], v[224:227], v[216:219], v[72:75]
	v_mfma_f32_16x16x32_bf16 v[68:71], v[232:235], v[216:219], v[68:71]
	s_setprio 0
	s_mov_b32 m0, s31
	s_barrier
	ds_read_b128 v[182:185], v153 offset:16384
	ds_read_b128 v[186:189], v153 offset:17408
	ds_read_b128 v[190:193], v153 offset:18432
	ds_read_b128 v[194:197], v153 offset:19456
	ds_read_b128 v[204:207], v153 offset:20480
	ds_read_b128 v[208:211], v153 offset:21504
	ds_read_b128 v[212:215], v153 offset:22528
	ds_read_b128 v[216:219], v153 offset:23552
	global_load_lds_dwordx4 v34, s[24:25]
	s_mov_b32 m0, s34
	v_mov_b32_e32 v163, v35
	global_load_lds_dwordx4 v162, s[24:25]
	s_barrier
	s_waitcnt lgkmcnt(0)
	v_lshl_add_u64 v[238:239], s[24:25], 0, v[34:35]
	v_lshl_add_u64 v[162:163], s[24:25], 0, v[162:163]
	s_setprio 1
	s_waitcnt lgkmcnt(0)
	v_mfma_f32_16x16x32_bf16 v[48:51], v[158:161], v[182:185], v[48:51]
	v_mfma_f32_16x16x32_bf16 v[44:47], v[174:177], v[182:185], v[44:47]
	v_mfma_f32_16x16x32_bf16 v[40:43], v[158:161], v[190:193], v[40:43]
	v_mfma_f32_16x16x32_bf16 v[36:39], v[174:177], v[190:193], v[36:39]
	v_mfma_f32_16x16x32_bf16 v[22:25], v[158:161], v[204:207], v[22:25]
	v_mfma_f32_16x16x32_bf16 v[18:21], v[174:177], v[204:207], v[18:21]
	v_mfma_f32_16x16x32_bf16 v[6:9], v[158:161], v[212:215], v[6:9]
	v_mfma_f32_16x16x32_bf16 v[2:5], v[174:177], v[212:215], v[2:5]
	v_mfma_f32_16x16x32_bf16 v[48:51], v[170:173], v[186:189], v[48:51]
	v_mfma_f32_16x16x32_bf16 v[44:47], v[178:181], v[186:189], v[44:47]
	v_mfma_f32_16x16x32_bf16 v[40:43], v[170:173], v[194:197], v[40:43]
	v_mfma_f32_16x16x32_bf16 v[36:39], v[178:181], v[194:197], v[36:39]
	v_mfma_f32_16x16x32_bf16 v[22:25], v[170:173], v[208:211], v[22:25]
	v_mfma_f32_16x16x32_bf16 v[18:21], v[178:181], v[208:211], v[18:21]
	v_mfma_f32_16x16x32_bf16 v[6:9], v[170:173], v[216:219], v[6:9]
	v_mfma_f32_16x16x32_bf16 v[2:5], v[178:181], v[216:219], v[2:5]
	s_setprio 0
	s_barrier
	s_add_u32 s46, s22, 0x40000
	s_addc_u32 s47, s23, 0
	s_add_i32 s45, s48, s30
	v_lshl_add_u64 v[158:159], s[46:47], 0, v[132:133]
	s_mov_b32 m0, s45
	s_nop 0
	global_load_lds_dwordx4 v[158:159], off
	v_lshl_add_u64 v[158:159], s[46:47], 0, v[134:135]
	s_add_i32 m0, s45, 0x2000
	s_nop 0
	global_load_lds_dwordx4 v[158:159], off
	s_waitcnt vmcnt(6)
	s_barrier
	s_setprio 1
	v_mfma_f32_16x16x32_bf16 v[30:33], v[220:223], v[182:185], v[30:33]
	v_mfma_f32_16x16x32_bf16 v[26:29], v[228:231], v[182:185], v[26:29]
	v_mfma_f32_16x16x32_bf16 v[14:17], v[220:223], v[190:193], v[14:17]
	v_mfma_f32_16x16x32_bf16 v[10:13], v[228:231], v[190:193], v[10:13]
	v_mfma_f32_16x16x32_bf16 v[60:63], v[220:223], v[204:207], v[60:63]
	v_mfma_f32_16x16x32_bf16 v[64:67], v[228:231], v[204:207], v[64:67]
	v_mfma_f32_16x16x32_bf16 v[52:55], v[220:223], v[212:215], v[52:55]
	v_mfma_f32_16x16x32_bf16 v[56:59], v[228:231], v[212:215], v[56:59]
	v_mfma_f32_16x16x32_bf16 v[30:33], v[224:227], v[186:189], v[30:33]
	v_mfma_f32_16x16x32_bf16 v[26:29], v[232:235], v[186:189], v[26:29]
	v_mfma_f32_16x16x32_bf16 v[14:17], v[224:227], v[194:197], v[14:17]
	v_mfma_f32_16x16x32_bf16 v[10:13], v[232:235], v[194:197], v[10:13]
	v_mfma_f32_16x16x32_bf16 v[60:63], v[224:227], v[208:211], v[60:63]
	v_mfma_f32_16x16x32_bf16 v[64:67], v[232:235], v[208:211], v[64:67]
	v_mfma_f32_16x16x32_bf16 v[52:55], v[224:227], v[216:219], v[52:55]
	v_mfma_f32_16x16x32_bf16 v[56:59], v[232:235], v[216:219], v[56:59]
	s_setprio 0
	s_add_i32 s45, 0, 0x18000
	v_add_u32_e32 v34, s45, v139
	s_barrier
	ds_read_b128 v[158:161], v34
	ds_read_b128 v[170:173], v34 offset:1024
	ds_read_b128 v[174:177], v34 offset:2048
	ds_read_b128 v[178:181], v34 offset:3072
	s_mov_b32 m0, s35
	ds_read_b128 v[182:185], v153 offset:32768
	ds_read_b128 v[186:189], v153 offset:33792
	ds_read_b128 v[190:193], v153 offset:34816
	ds_read_b128 v[194:197], v153 offset:35840
	ds_read_b128 v[204:207], v153 offset:36864
	ds_read_b128 v[208:211], v153 offset:37888
	ds_read_b128 v[212:215], v153 offset:38912
	ds_read_b128 v[216:219], v153 offset:39936
	global_load_lds_dwordx4 v141, s[24:25]
	s_mov_b32 m0, s36
	s_nop 0
	global_load_lds_dwordx4 v143, s[24:25]
	s_waitcnt lgkmcnt(8)
	s_barrier
	s_waitcnt lgkmcnt(0)
	s_setprio 1
	s_waitcnt lgkmcnt(0)
	v_mfma_f32_16x16x32_bf16 v[128:131], v[158:161], v[182:185], v[128:131]
	v_mfma_f32_16x16x32_bf16 v[124:127], v[174:177], v[182:185], v[124:127]
	v_mfma_f32_16x16x32_bf16 v[120:123], v[158:161], v[190:193], v[120:123]
	v_mfma_f32_16x16x32_bf16 v[116:119], v[174:177], v[190:193], v[116:119]
	v_mfma_f32_16x16x32_bf16 v[104:107], v[158:161], v[204:207], v[104:107]
	v_mfma_f32_16x16x32_bf16 v[100:103], v[174:177], v[204:207], v[100:103]
	v_mfma_f32_16x16x32_bf16 v[88:91], v[158:161], v[212:215], v[88:91]
	v_mfma_f32_16x16x32_bf16 v[84:87], v[174:177], v[212:215], v[84:87]
	v_mfma_f32_16x16x32_bf16 v[128:131], v[170:173], v[186:189], v[128:131]
	v_mfma_f32_16x16x32_bf16 v[124:127], v[178:181], v[186:189], v[124:127]
	v_mfma_f32_16x16x32_bf16 v[120:123], v[170:173], v[194:197], v[120:123]
	v_mfma_f32_16x16x32_bf16 v[116:119], v[178:181], v[194:197], v[116:119]
	v_mfma_f32_16x16x32_bf16 v[104:107], v[170:173], v[208:211], v[104:107]
	v_mfma_f32_16x16x32_bf16 v[100:103], v[178:181], v[208:211], v[100:103]
	v_mfma_f32_16x16x32_bf16 v[88:91], v[170:173], v[216:219], v[88:91]
	v_mfma_f32_16x16x32_bf16 v[84:87], v[178:181], v[216:219], v[84:87]
	s_setprio 0
	s_barrier
	s_add_i32 s24, 0, 0x1c000
	s_add_i32 s25, s45, s30
	v_add_u32_e32 v34, s24, v139
	v_lshl_add_u64 v[198:199], v[198:199], 0, s[20:21]
	s_mov_b32 m0, s25
	ds_read_b128 v[220:223], v34
	ds_read_b128 v[224:227], v34 offset:1024
	ds_read_b128 v[228:231], v34 offset:2048
	ds_read_b128 v[232:235], v34 offset:3072
	global_load_lds_dwordx4 v[198:199], off
	v_lshl_add_u64 v[198:199], v[236:237], 0, s[20:21]
	s_add_i32 m0, s25, 0x2000
	s_nop 0
	global_load_lds_dwordx4 v[198:199], off
	s_barrier
	s_waitcnt lgkmcnt(0)
	s_setprio 1
	s_waitcnt lgkmcnt(0)
	v_mfma_f32_16x16x32_bf16 v[112:115], v[220:223], v[182:185], v[112:115]
	v_mfma_f32_16x16x32_bf16 v[108:111], v[228:231], v[182:185], v[108:111]
	v_mfma_f32_16x16x32_bf16 v[96:99], v[220:223], v[190:193], v[96:99]
	v_mfma_f32_16x16x32_bf16 v[92:95], v[228:231], v[190:193], v[92:95]
	v_mfma_f32_16x16x32_bf16 v[80:83], v[220:223], v[204:207], v[80:83]
	v_mfma_f32_16x16x32_bf16 v[76:79], v[228:231], v[204:207], v[76:79]
	v_mfma_f32_16x16x32_bf16 v[72:75], v[220:223], v[212:215], v[72:75]
	v_mfma_f32_16x16x32_bf16 v[68:71], v[228:231], v[212:215], v[68:71]
	v_mfma_f32_16x16x32_bf16 v[112:115], v[224:227], v[186:189], v[112:115]
	v_mfma_f32_16x16x32_bf16 v[108:111], v[232:235], v[186:189], v[108:111]
	v_mfma_f32_16x16x32_bf16 v[96:99], v[224:227], v[194:197], v[96:99]
	v_mfma_f32_16x16x32_bf16 v[92:95], v[232:235], v[194:197], v[92:95]
	v_mfma_f32_16x16x32_bf16 v[80:83], v[224:227], v[208:211], v[80:83]
	v_mfma_f32_16x16x32_bf16 v[76:79], v[232:235], v[208:211], v[76:79]
	v_mfma_f32_16x16x32_bf16 v[72:75], v[224:227], v[216:219], v[72:75]
	v_mfma_f32_16x16x32_bf16 v[68:71], v[232:235], v[216:219], v[68:71]
	s_setprio 0
	s_mov_b32 m0, s37
	v_lshl_add_u64 v[198:199], v[238:239], 0, s[20:21]
	s_barrier
	ds_read_b128 v[182:185], v153 offset:49152
	ds_read_b128 v[186:189], v153 offset:50176
	ds_read_b128 v[190:193], v153 offset:51200
	ds_read_b128 v[194:197], v153 offset:52224
	ds_read_b128 v[204:207], v153 offset:53248
	ds_read_b128 v[208:211], v153 offset:54272
	ds_read_b128 v[212:215], v153 offset:55296
	ds_read_b128 v[216:219], v153 offset:56320
	global_load_lds_dwordx4 v[198:199], off
	v_lshl_add_u64 v[162:163], v[162:163], 0, s[20:21]
	s_mov_b32 m0, s38
	s_nop 0
	global_load_lds_dwordx4 v[162:163], off
	s_barrier
	s_waitcnt lgkmcnt(0)
	s_setprio 1
	s_waitcnt lgkmcnt(0)
	v_mfma_f32_16x16x32_bf16 v[48:51], v[158:161], v[182:185], v[48:51]
	v_mfma_f32_16x16x32_bf16 v[44:47], v[174:177], v[182:185], v[44:47]
	v_mfma_f32_16x16x32_bf16 v[40:43], v[158:161], v[190:193], v[40:43]
	v_mfma_f32_16x16x32_bf16 v[36:39], v[174:177], v[190:193], v[36:39]
	v_mfma_f32_16x16x32_bf16 v[22:25], v[158:161], v[204:207], v[22:25]
	v_mfma_f32_16x16x32_bf16 v[18:21], v[174:177], v[204:207], v[18:21]
	v_mfma_f32_16x16x32_bf16 v[6:9], v[158:161], v[212:215], v[6:9]
	v_mfma_f32_16x16x32_bf16 v[2:5], v[174:177], v[212:215], v[2:5]
	v_mfma_f32_16x16x32_bf16 v[48:51], v[170:173], v[186:189], v[48:51]
	v_mfma_f32_16x16x32_bf16 v[44:47], v[178:181], v[186:189], v[44:47]
	v_mfma_f32_16x16x32_bf16 v[40:43], v[170:173], v[194:197], v[40:43]
	v_mfma_f32_16x16x32_bf16 v[36:39], v[178:181], v[194:197], v[36:39]
	v_mfma_f32_16x16x32_bf16 v[22:25], v[170:173], v[208:211], v[22:25]
	v_mfma_f32_16x16x32_bf16 v[18:21], v[178:181], v[208:211], v[18:21]
	v_mfma_f32_16x16x32_bf16 v[6:9], v[170:173], v[216:219], v[6:9]
	v_mfma_f32_16x16x32_bf16 v[2:5], v[178:181], v[216:219], v[2:5]
	s_setprio 0
	s_barrier
	s_add_u32 s22, s22, 0x40080
	s_addc_u32 s23, s23, 0
	s_add_i32 s24, s24, s30
	v_lshl_add_u64 v[158:159], s[22:23], 0, v[132:133]
	s_mov_b32 m0, s24
	s_nop 0
	global_load_lds_dwordx4 v[158:159], off
	v_lshl_add_u64 v[158:159], s[22:23], 0, v[134:135]
	s_add_i32 m0, s24, 0x2000
	s_nop 0
	global_load_lds_dwordx4 v[158:159], off
	s_waitcnt vmcnt(6)
	s_barrier
	s_setprio 1
	v_mfma_f32_16x16x32_bf16 v[30:33], v[220:223], v[182:185], v[30:33]
	v_mfma_f32_16x16x32_bf16 v[26:29], v[228:231], v[182:185], v[26:29]
	v_mfma_f32_16x16x32_bf16 v[14:17], v[220:223], v[190:193], v[14:17]
	v_mfma_f32_16x16x32_bf16 v[10:13], v[228:231], v[190:193], v[10:13]
	v_mfma_f32_16x16x32_bf16 v[60:63], v[220:223], v[204:207], v[60:63]
	v_mfma_f32_16x16x32_bf16 v[64:67], v[228:231], v[204:207], v[64:67]
	v_mfma_f32_16x16x32_bf16 v[52:55], v[220:223], v[212:215], v[52:55]
	v_mfma_f32_16x16x32_bf16 v[56:59], v[228:231], v[212:215], v[56:59]
	v_mfma_f32_16x16x32_bf16 v[30:33], v[224:227], v[186:189], v[30:33]
	v_mfma_f32_16x16x32_bf16 v[26:29], v[232:235], v[186:189], v[26:29]
	v_mfma_f32_16x16x32_bf16 v[14:17], v[224:227], v[194:197], v[14:17]
	v_mfma_f32_16x16x32_bf16 v[10:13], v[232:235], v[194:197], v[10:13]
	v_mfma_f32_16x16x32_bf16 v[60:63], v[224:227], v[208:211], v[60:63]
	v_mfma_f32_16x16x32_bf16 v[64:67], v[232:235], v[208:211], v[64:67]
	v_mfma_f32_16x16x32_bf16 v[52:55], v[224:227], v[216:219], v[52:55]
	v_mfma_f32_16x16x32_bf16 v[56:59], v[232:235], v[216:219], v[56:59]
	s_setprio 0
	s_add_i32 s44, s44, 2
	s_add_u32 s4, s4, 0x100
	s_addc_u32 s5, s5, 0
	s_cmp_gt_u32 s44, 13
	s_barrier
	s_cbranch_scc0 .LBB0_158
	v_lshl_add_u32 v34, s42, 8, v137
	v_lshl_or_b32 v140, s41, 8, v152
	v_ashrrev_i32_e32 v141, 31, v140
	v_mov_b64_e32 v[142:143], s[8:9]
	v_cvt_pk_bf16_f32 v72, v72, v73
	v_cvt_pk_bf16_f32 v73, v74, v75
	v_cvt_pk_bf16_f32 v74, v68, v69
	v_add_u32_e32 v68, 0x80, v34
	v_lshlrev_b64 v[140:141], 1, v[140:141]
	v_mad_i64_i32 v[68:69], s[0:1], v68, s90, v[142:143]
	v_cvt_pk_bf16_f32 v30, v30, v31
	v_cvt_pk_bf16_f32 v31, v32, v33
	v_cvt_pk_bf16_f32 v32, v26, v27
	v_add_u32_e32 v26, 0x90, v34
	v_lshl_add_u64 v[68:69], v[68:69], 0, v[140:141]
	v_cvt_pk_bf16_f32 v33, v28, v29
	v_mad_i64_i32 v[26:27], s[0:1], v26, s90, v[142:143]
	v_cvt_pk_bf16_f32 v14, v14, v15
	v_cvt_pk_bf16_f32 v15, v16, v17
	v_cvt_pk_bf16_f32 v16, v10, v11
	v_add_u32_e32 v10, 0xa0, v34
	global_store_dwordx4 v[68:69], v[30:33], off offset:256 nt
	v_cvt_pk_bf16_f32 v17, v12, v13
	v_mad_i64_i32 v[10:11], s[0:1], v10, s90, v[142:143]
	v_lshl_add_u64 v[30:31], v[26:27], 0, v[140:141]
	v_mad_i64_i32 v[144:145], s[0:1], v34, s90, v[142:143]
	v_cvt_pk_bf16_f32 v112, v112, v113
	v_cvt_pk_bf16_f32 v113, v114, v115
	v_cvt_pk_bf16_f32 v114, v108, v109
	v_or_b32_e32 v108, 16, v34
	global_store_dwordx4 v[30:31], v[14:17], off offset:256 nt
	v_cvt_pk_bf16_f32 v12, v18, v19
	v_cvt_pk_bf16_f32 v13, v20, v21
	v_lshl_add_u64 v[14:15], v[10:11], 0, v[140:141]
	v_cvt_pk_bf16_f32 v10, v22, v23
	v_cvt_pk_bf16_f32 v11, v24, v25
	v_lshl_add_u64 v[144:145], v[144:145], 0, v[140:141]
	v_cvt_pk_bf16_f32 v115, v110, v111
	v_mad_i64_i32 v[108:109], s[0:1], v108, s90, v[142:143]
	v_cvt_pk_bf16_f32 v96, v96, v97
	v_cvt_pk_bf16_f32 v97, v98, v99
	v_cvt_pk_bf16_f32 v98, v92, v93
	v_or_b32_e32 v92, 32, v34
	global_store_dwordx4 v[14:15], v[10:13], off nt
	global_store_dwordx4 v[144:145], v[112:115], off offset:256 nt
	v_cvt_pk_bf16_f32 v99, v94, v95
	v_cvt_pk_bf16_f32 v10, v60, v61
	v_cvt_pk_bf16_f32 v11, v62, v63
	v_cvt_pk_bf16_f32 v12, v64, v65
	v_cvt_pk_bf16_f32 v13, v66, v67
	v_lshl_add_u64 v[112:113], v[108:109], 0, v[140:141]
	v_mad_i64_i32 v[92:93], s[0:1], v92, s90, v[142:143]
	v_cvt_pk_bf16_f32 v80, v80, v81
	v_cvt_pk_bf16_f32 v81, v82, v83
	v_cvt_pk_bf16_f32 v82, v76, v77
	v_or_b32_e32 v76, 48, v34
	global_store_dwordx4 v[14:15], v[10:13], off offset:256 nt
	global_store_dwordx4 v[112:113], v[96:99], off offset:256 nt
	v_cvt_pk_bf16_f32 v83, v78, v79
	v_add_u32_e32 v10, 0xb0, v34
	v_lshl_add_u64 v[96:97], v[92:93], 0, v[140:141]
	v_mad_i64_i32 v[76:77], s[0:1], v76, s90, v[142:143]
	v_mad_i64_i32 v[10:11], s[0:1], v10, s90, v[142:143]
	v_cvt_pk_bf16_f32 v128, v128, v129
	v_cvt_pk_bf16_f32 v129, v130, v131
	v_cvt_pk_bf16_f32 v130, v124, v125
	v_cvt_pk_bf16_f32 v131, v126, v127
	v_cvt_pk_bf16_f32 v108, v120, v121
	v_cvt_pk_bf16_f32 v109, v122, v123
	v_cvt_pk_bf16_f32 v110, v116, v117
	v_cvt_pk_bf16_f32 v111, v118, v119
	v_cvt_pk_bf16_f32 v92, v104, v105
	v_cvt_pk_bf16_f32 v93, v106, v107
	v_cvt_pk_bf16_f32 v94, v100, v101
	v_cvt_pk_bf16_f32 v95, v102, v103
	global_store_dwordx4 v[96:97], v[80:83], off offset:256 nt
	v_cvt_pk_bf16_f32 v78, v84, v85
	v_cvt_pk_bf16_f32 v79, v86, v87
	v_lshl_add_u64 v[80:81], v[76:77], 0, v[140:141]
	v_cvt_pk_bf16_f32 v76, v88, v89
	v_cvt_pk_bf16_f32 v77, v90, v91
	v_cvt_pk_bf16_f32 v75, v70, v71
	v_cvt_pk_bf16_f32 v48, v48, v49
	v_cvt_pk_bf16_f32 v49, v50, v51
	v_cvt_pk_bf16_f32 v50, v44, v45
	v_cvt_pk_bf16_f32 v51, v46, v47
	v_cvt_pk_bf16_f32 v26, v40, v41
	v_cvt_pk_bf16_f32 v27, v42, v43
	v_cvt_pk_bf16_f32 v28, v36, v37
	v_cvt_pk_bf16_f32 v29, v38, v39
	v_lshl_add_u64 v[10:11], v[10:11], 0, v[140:141]
	v_cvt_pk_bf16_f32 v6, v6, v7
	v_cvt_pk_bf16_f32 v7, v8, v9
	v_cvt_pk_bf16_f32 v8, v2, v3
	v_cvt_pk_bf16_f32 v9, v4, v5
	v_cvt_pk_bf16_f32 v2, v52, v53
	v_cvt_pk_bf16_f32 v3, v54, v55
	v_cvt_pk_bf16_f32 v4, v56, v57
	v_cvt_pk_bf16_f32 v5, v58, v59
	s_and_b64 vcc, exec, s[2:3]
	v_mov_b32_e32 v142, v157
	v_mov_b32_e32 v140, v156
	v_mov_b32_e32 v138, v155
	v_mov_b32_e32 v136, v154
	s_mov_b32 s41, s14
	s_mov_b32 s42, s40
	s_mov_b64 s[22:23], s[18:19]
	global_store_dwordx4 v[144:145], v[128:131], off nt
	global_store_dwordx4 v[112:113], v[108:111], off nt
	global_store_dwordx4 v[96:97], v[92:95], off nt
	global_store_dwordx4 v[80:81], v[76:79], off nt
	global_store_dwordx4 v[80:81], v[72:75], off offset:256 nt
	global_store_dwordx4 v[68:69], v[48:51], off nt
	global_store_dwordx4 v[30:31], v[26:29], off nt
	global_store_dwordx4 v[10:11], v[6:9], off nt
	global_store_dwordx4 v[10:11], v[2:5], off offset:256 nt
	s_cbranch_vccz .LBB0_149
	s_waitcnt vmcnt(0)
	s_cmpk_gt_u32 s27, 0xff
	s_cbranch_scc1 .LBB0_162
	s_barrier
